# V phase second half-trip: 8 register copies removed (high-half operand select for odd-register weights, renamed accumulator, loop-carried accumulator written directly)
# speedup vs baseline: 1.0105x; 1.0042x over previous
.LBB0_956:
	s_and_b32 s8, s3, 0x78
	s_add_i32 s8, s8, s4
	s_ashr_i32 s9, s8, 31
	s_lshl_b64 s[10:11], s[8:9], 15
	s_add_u32 s10, s12, s10
	s_addc_u32 s11, s13, s11
	s_and_b32 s17, s16, 0x1000
	s_lshl_b32 s17, s17, 2
	s_add_u32 s10, s10, s17
	s_addc_u32 s11, s11, 0
	s_add_u32 s62, s10, s6
	s_addc_u32 s63, s11, s7
	s_add_u32 s64, s10, s14
	s_addc_u32 s65, s11, 0
	s_mov_b32 s17, s18
	s_nop 0
	global_load_dword v104, v2, s[62:63] offset:256
	global_load_dword v106, v2, s[62:63] offset:512
	global_load_dword v108, v2, s[62:63] offset:768
	global_load_dword v110, v2, s[62:63] offset:1024
	global_load_dword v112, v2, s[62:63] offset:1280
	global_load_dword v114, v2, s[62:63] offset:1536
	global_load_dword v98, v2, s[62:63] offset:1792
	global_load_dword v100, v2, s[62:63] offset:2048
	global_load_dword v116, v2, s[64:65] offset:-4096
	global_load_dword v102, v2, s[62:63] offset:2304
	global_load_dword v78, v2, s[62:63] offset:2560
	global_load_dword v80, v2, s[62:63] offset:2816
	global_load_dword v82, v2, s[62:63] offset:3072
	global_load_dword v84, v2, s[62:63] offset:3328
	global_load_dword v86, v2, s[62:63] offset:3584
	global_load_dword v88, v2, s[62:63] offset:3840
	global_load_dword v90, v2, s[64:65]
	global_load_dword v92, v2, s[64:65] offset:256
	global_load_dword v94, v2, s[64:65] offset:512
	global_load_dword v96, v2, s[64:65] offset:768
	global_load_dword v76, v2, s[64:65] offset:1024
	global_load_dword v77, v2, s[64:65] offset:1280
	global_load_dword v56, v2, s[64:65] offset:1536
	global_load_dword v57, v2, s[64:65] offset:1792
	global_load_dword v58, v2, s[64:65] offset:2048
	global_load_dword v59, v2, s[64:65] offset:2304
	global_load_dword v60, v2, s[64:65] offset:2560
	global_load_dword v61, v2, s[64:65] offset:2816
	global_load_dword v62, v2, s[64:65] offset:3072
	global_load_dword v63, v2, s[64:65] offset:3328
	global_load_dword v54, v2, s[64:65] offset:3584
	global_load_dword v55, v2, s[64:65] offset:3840
	s_waitcnt vmcnt(56)
	v_and_b32_e32 v9, 0x1fff8, v64
	v_and_b32_e32 v11, 0x1fff8, v66
	v_and_b32_e32 v13, 0x1fff8, v68
	v_and_b32_e32 v15, 0x1fff8, v70
	ds_read_b64 v[126:127], v9
	ds_read_b64 v[128:129], v11
	ds_read_b64 v[130:131], v13
	ds_read_b64 v[132:133], v15
	v_and_b32_e32 v9, 0x1fff8, v72
	v_and_b32_e32 v11, 0x1fff8, v74
	v_and_b32_e32 v13, 0x1fff8, v48
	v_and_b32_e32 v15, 0x1fff8, v50
	ds_read_b64 v[134:135], v9
	ds_read_b64 v[136:137], v11
	ds_read_b64 v[138:139], v13
	ds_read_b64 v[140:141], v15
	s_setprio 1
	s_waitcnt lgkmcnt(7)
	v_cvt_pk_f32_fp8_e32 v[142:143], v126
	v_cvt_pk_f32_fp8_sdwa v[144:145], v126 src0_sel:WORD_1
	v_cvt_pk_f32_fp8_e32 v[146:147], v127
	v_cvt_pk_f32_fp8_sdwa v[126:127], v127 src0_sel:WORD_1
	s_waitcnt lgkmcnt(6)
	v_cvt_pk_f32_fp8_e32 v[148:149], v128
	v_cvt_pk_f32_fp8_sdwa v[150:151], v128 src0_sel:WORD_1
	v_cvt_pk_f32_fp8_e32 v[152:153], v129
	v_cvt_pk_f32_fp8_sdwa v[128:129], v129 src0_sel:WORD_1
	s_waitcnt lgkmcnt(5)
	v_cvt_pk_f32_fp8_e32 v[154:155], v130
	v_cvt_pk_f32_fp8_sdwa v[156:157], v130 src0_sel:WORD_1
	v_cvt_pk_f32_fp8_e32 v[158:159], v131
	v_cvt_pk_f32_fp8_sdwa v[130:131], v131 src0_sel:WORD_1
	s_waitcnt lgkmcnt(4)
	v_cvt_pk_f32_fp8_e32 v[160:161], v132
	v_cvt_pk_f32_fp8_sdwa v[162:163], v132 src0_sel:WORD_1
	v_cvt_pk_f32_fp8_e32 v[164:165], v133
	v_cvt_pk_f32_fp8_sdwa v[132:133], v133 src0_sel:WORD_1
	s_waitcnt lgkmcnt(3)
	v_cvt_pk_f32_fp8_e32 v[166:167], v134
	v_cvt_pk_f32_fp8_sdwa v[168:169], v134 src0_sel:WORD_1
	v_cvt_pk_f32_fp8_e32 v[170:171], v135
	v_cvt_pk_f32_fp8_sdwa v[134:135], v135 src0_sel:WORD_1
	s_waitcnt lgkmcnt(2)
	v_cvt_pk_f32_fp8_e32 v[172:173], v136
	v_cvt_pk_f32_fp8_sdwa v[174:175], v136 src0_sel:WORD_1
	v_cvt_pk_f32_fp8_e32 v[176:177], v137
	v_cvt_pk_f32_fp8_sdwa v[136:137], v137 src0_sel:WORD_1
	s_waitcnt lgkmcnt(1)
	v_cvt_pk_f32_fp8_e32 v[178:179], v138
	v_cvt_pk_f32_fp8_sdwa v[180:181], v138 src0_sel:WORD_1
	v_cvt_pk_f32_fp8_e32 v[182:183], v139
	v_cvt_pk_f32_fp8_sdwa v[138:139], v139 src0_sel:WORD_1
	s_waitcnt lgkmcnt(0)
	v_cvt_pk_f32_fp8_e32 v[184:185], v140
	v_cvt_pk_f32_fp8_sdwa v[186:187], v140 src0_sel:WORD_1
	v_cvt_pk_f32_fp8_e32 v[188:189], v141
	v_cvt_pk_f32_fp8_sdwa v[140:141], v141 src0_sel:WORD_1
	s_setprio 0
	s_waitcnt vmcnt(48)
	v_and_b32_e32 v9, 0x1fff8, v52
	v_and_b32_e32 v11, 0x1fff8, v32
	v_and_b32_e32 v13, 0x1fff8, v34
	v_and_b32_e32 v15, 0x1fff8, v36
	ds_read_b64 v[190:191], v9
	ds_read_b64 v[192:193], v11
	ds_read_b64 v[194:195], v13
	ds_read_b64 v[196:197], v15
	v_and_b32_e32 v9, 0x1fff8, v38
	v_and_b32_e32 v11, 0x1fff8, v40
	v_and_b32_e32 v13, 0x1fff8, v42
	v_and_b32_e32 v15, 0x1fff8, v44
	ds_read_b64 v[198:199], v9
	ds_read_b64 v[200:201], v11
	ds_read_b64 v[202:203], v13
	ds_read_b64 v[204:205], v15
	s_setprio 1
	v_pk_fma_f32 v[118:119], v[142:143], v[64:65], v[118:119] op_sel_hi:[1,0,1]
	v_pk_fma_f32 v[122:123], v[144:145], v[64:65], v[122:123] op_sel_hi:[1,0,1]
	v_pk_fma_f32 v[120:121], v[146:147], v[64:65], v[120:121] op_sel_hi:[1,0,1]
	v_pk_fma_f32 v[64:65], v[126:127], v[64:65], v[124:125] op_sel_hi:[1,0,1]
	v_pk_fma_f32 v[118:119], v[148:149], v[66:67], v[118:119] op_sel_hi:[1,0,1]
	v_pk_fma_f32 v[122:123], v[150:151], v[66:67], v[122:123] op_sel_hi:[1,0,1]
	v_pk_fma_f32 v[120:121], v[152:153], v[66:67], v[120:121] op_sel_hi:[1,0,1]
	v_pk_fma_f32 v[64:65], v[128:129], v[66:67], v[64:65] op_sel_hi:[1,0,1]
	v_pk_fma_f32 v[118:119], v[154:155], v[68:69], v[118:119] op_sel_hi:[1,0,1]
	v_pk_fma_f32 v[122:123], v[156:157], v[68:69], v[122:123] op_sel_hi:[1,0,1]
	v_pk_fma_f32 v[120:121], v[158:159], v[68:69], v[120:121] op_sel_hi:[1,0,1]
	v_pk_fma_f32 v[64:65], v[130:131], v[68:69], v[64:65] op_sel_hi:[1,0,1]
	v_pk_fma_f32 v[118:119], v[160:161], v[70:71], v[118:119] op_sel_hi:[1,0,1]
	v_pk_fma_f32 v[122:123], v[162:163], v[70:71], v[122:123] op_sel_hi:[1,0,1]
	v_pk_fma_f32 v[120:121], v[164:165], v[70:71], v[120:121] op_sel_hi:[1,0,1]
	v_pk_fma_f32 v[64:65], v[132:133], v[70:71], v[64:65] op_sel_hi:[1,0,1]
	s_waitcnt lgkmcnt(7)
	v_cvt_pk_f32_fp8_e32 v[206:207], v190
	v_cvt_pk_f32_fp8_sdwa v[208:209], v190 src0_sel:WORD_1
	v_cvt_pk_f32_fp8_e32 v[210:211], v191
	v_cvt_pk_f32_fp8_sdwa v[190:191], v191 src0_sel:WORD_1
	v_pk_fma_f32 v[118:119], v[166:167], v[72:73], v[118:119] op_sel_hi:[1,0,1]
	v_pk_fma_f32 v[122:123], v[168:169], v[72:73], v[122:123] op_sel_hi:[1,0,1]
	v_pk_fma_f32 v[120:121], v[170:171], v[72:73], v[120:121] op_sel_hi:[1,0,1]
	v_pk_fma_f32 v[64:65], v[134:135], v[72:73], v[64:65] op_sel_hi:[1,0,1]
	v_pk_fma_f32 v[118:119], v[172:173], v[74:75], v[118:119] op_sel_hi:[1,0,1]
	v_pk_fma_f32 v[122:123], v[174:175], v[74:75], v[122:123] op_sel_hi:[1,0,1]
	v_pk_fma_f32 v[120:121], v[176:177], v[74:75], v[120:121] op_sel_hi:[1,0,1]
	v_pk_fma_f32 v[64:65], v[136:137], v[74:75], v[64:65] op_sel_hi:[1,0,1]
	s_waitcnt lgkmcnt(6)
	v_cvt_pk_f32_fp8_e32 v[66:67], v192
	v_cvt_pk_f32_fp8_sdwa v[68:69], v192 src0_sel:WORD_1
	v_cvt_pk_f32_fp8_e32 v[70:71], v193
	v_cvt_pk_f32_fp8_sdwa v[72:73], v193 src0_sel:WORD_1
	s_waitcnt lgkmcnt(5)
	v_cvt_pk_f32_fp8_e32 v[74:75], v194
	v_cvt_pk_f32_fp8_sdwa v[124:125], v194 src0_sel:WORD_1
	v_pk_fma_f32 v[118:119], v[178:179], v[48:49], v[118:119] op_sel_hi:[1,0,1]
	v_pk_fma_f32 v[122:123], v[180:181], v[48:49], v[122:123] op_sel_hi:[1,0,1]
	v_pk_fma_f32 v[120:121], v[182:183], v[48:49], v[120:121] op_sel_hi:[1,0,1]
	v_pk_fma_f32 v[48:49], v[138:139], v[48:49], v[64:65] op_sel_hi:[1,0,1]
	v_pk_fma_f32 v[118:119], v[184:185], v[50:51], v[118:119] op_sel_hi:[1,0,1]
	v_pk_fma_f32 v[122:123], v[186:187], v[50:51], v[122:123] op_sel_hi:[1,0,1]
	v_pk_fma_f32 v[120:121], v[188:189], v[50:51], v[120:121] op_sel_hi:[1,0,1]
	v_pk_fma_f32 v[48:49], v[140:141], v[50:51], v[48:49] op_sel_hi:[1,0,1]
	v_pk_fma_f32 v[118:119], v[206:207], v[52:53], v[118:119] op_sel_hi:[1,0,1]
	v_pk_fma_f32 v[122:123], v[208:209], v[52:53], v[122:123] op_sel_hi:[1,0,1]
	v_pk_fma_f32 v[120:121], v[210:211], v[52:53], v[120:121] op_sel_hi:[1,0,1]
	v_pk_fma_f32 v[48:49], v[190:191], v[52:53], v[48:49] op_sel_hi:[1,0,1]
	v_cvt_pk_f32_fp8_e32 v[126:127], v195
	v_cvt_pk_f32_fp8_sdwa v[128:129], v195 src0_sel:WORD_1
	s_waitcnt lgkmcnt(4)
	v_cvt_pk_f32_fp8_e32 v[130:131], v196
	v_cvt_pk_f32_fp8_sdwa v[132:133], v196 src0_sel:WORD_1
	v_cvt_pk_f32_fp8_e32 v[134:135], v197
	v_cvt_pk_f32_fp8_sdwa v[136:137], v197 src0_sel:WORD_1
	s_waitcnt lgkmcnt(3)
	v_cvt_pk_f32_fp8_e32 v[142:143], v198
	v_cvt_pk_f32_fp8_sdwa v[144:145], v198 src0_sel:WORD_1
	v_cvt_pk_f32_fp8_e32 v[146:147], v199
	v_cvt_pk_f32_fp8_sdwa v[148:149], v199 src0_sel:WORD_1
	s_waitcnt lgkmcnt(2)
	v_cvt_pk_f32_fp8_e32 v[150:151], v200
	v_cvt_pk_f32_fp8_sdwa v[152:153], v200 src0_sel:WORD_1
	v_cvt_pk_f32_fp8_e32 v[154:155], v201
	v_cvt_pk_f32_fp8_sdwa v[156:157], v201 src0_sel:WORD_1
	s_waitcnt lgkmcnt(1)
	v_cvt_pk_f32_fp8_e32 v[158:159], v202
	v_cvt_pk_f32_fp8_sdwa v[160:161], v202 src0_sel:WORD_1
	v_cvt_pk_f32_fp8_e32 v[162:163], v203
	v_cvt_pk_f32_fp8_sdwa v[164:165], v203 src0_sel:WORD_1
	s_waitcnt lgkmcnt(0)
	v_cvt_pk_f32_fp8_e32 v[166:167], v204
	v_cvt_pk_f32_fp8_sdwa v[168:169], v204 src0_sel:WORD_1
	v_cvt_pk_f32_fp8_e32 v[170:171], v205
	v_cvt_pk_f32_fp8_sdwa v[172:173], v205 src0_sel:WORD_1
	s_setprio 0
	s_waitcnt vmcnt(40)
	v_and_b32_e32 v9, 0x1fff8, v46
	v_and_b32_e32 v11, 0x1fff8, v26
	v_and_b32_e32 v13, 0x1fff8, v28
	v_and_b32_e32 v15, 0x1fff8, v30
	ds_read_b64 v[50:51], v9
	ds_read_b64 v[52:53], v11
	ds_read_b64 v[64:65], v13
	ds_read_b64 v[138:139], v15
	v_and_b32_e32 v9, 0x1fff8, v4
	v_and_b32_e32 v11, 0x1fff8, v6
	v_and_b32_e32 v13, 0x1fff8, v8
	v_and_b32_e32 v15, 0x1fff8, v10
	ds_read_b64 v[140:141], v9
	ds_read_b64 v[174:175], v11
	ds_read_b64 v[176:177], v13
	ds_read_b64 v[178:179], v15
	s_setprio 1
	v_pk_fma_f32 v[66:67], v[66:67], v[32:33], v[118:119] op_sel_hi:[1,0,1]
	v_pk_fma_f32 v[68:69], v[68:69], v[32:33], v[122:123] op_sel_hi:[1,0,1]
	v_pk_fma_f32 v[70:71], v[70:71], v[32:33], v[120:121] op_sel_hi:[1,0,1]
	v_pk_fma_f32 v[32:33], v[72:73], v[32:33], v[48:49] op_sel_hi:[1,0,1]
	v_pk_fma_f32 v[66:67], v[74:75], v[34:35], v[66:67] op_sel_hi:[1,0,1]
	v_pk_fma_f32 v[68:69], v[124:125], v[34:35], v[68:69] op_sel_hi:[1,0,1]
	v_pk_fma_f32 v[70:71], v[126:127], v[34:35], v[70:71] op_sel_hi:[1,0,1]
	v_pk_fma_f32 v[32:33], v[128:129], v[34:35], v[32:33] op_sel_hi:[1,0,1]
	v_pk_fma_f32 v[66:67], v[130:131], v[36:37], v[66:67] op_sel_hi:[1,0,1]
	v_pk_fma_f32 v[68:69], v[132:133], v[36:37], v[68:69] op_sel_hi:[1,0,1]
	v_pk_fma_f32 v[70:71], v[134:135], v[36:37], v[70:71] op_sel_hi:[1,0,1]
	v_pk_fma_f32 v[32:33], v[136:137], v[36:37], v[32:33] op_sel_hi:[1,0,1]
	s_waitcnt lgkmcnt(7)
	v_cvt_pk_f32_fp8_e32 v[180:181], v50
	v_cvt_pk_f32_fp8_sdwa v[182:183], v50 src0_sel:WORD_1
	v_cvt_pk_f32_fp8_e32 v[184:185], v51
	v_cvt_pk_f32_fp8_sdwa v[50:51], v51 src0_sel:WORD_1
	v_pk_fma_f32 v[66:67], v[142:143], v[38:39], v[66:67] op_sel_hi:[1,0,1]
	v_pk_fma_f32 v[68:69], v[144:145], v[38:39], v[68:69] op_sel_hi:[1,0,1]
	v_pk_fma_f32 v[70:71], v[146:147], v[38:39], v[70:71] op_sel_hi:[1,0,1]
	v_pk_fma_f32 v[32:33], v[148:149], v[38:39], v[32:33] op_sel_hi:[1,0,1]
	s_waitcnt lgkmcnt(6)
	v_cvt_pk_f32_fp8_e32 v[186:187], v52
	v_cvt_pk_f32_fp8_sdwa v[188:189], v52 src0_sel:WORD_1
	v_cvt_pk_f32_fp8_e32 v[190:191], v53
	v_cvt_pk_f32_fp8_sdwa v[52:53], v53 src0_sel:WORD_1
	v_pk_fma_f32 v[66:67], v[150:151], v[40:41], v[66:67] op_sel_hi:[1,0,1]
	v_pk_fma_f32 v[68:69], v[152:153], v[40:41], v[68:69] op_sel_hi:[1,0,1]
	v_pk_fma_f32 v[70:71], v[154:155], v[40:41], v[70:71] op_sel_hi:[1,0,1]
	v_pk_fma_f32 v[32:33], v[156:157], v[40:41], v[32:33] op_sel_hi:[1,0,1]
	s_waitcnt lgkmcnt(5)
	v_cvt_pk_f32_fp8_e32 v[192:193], v64
	v_cvt_pk_f32_fp8_sdwa v[194:195], v64 src0_sel:WORD_1
	v_cvt_pk_f32_fp8_e32 v[196:197], v65
	v_cvt_pk_f32_fp8_sdwa v[64:65], v65 src0_sel:WORD_1
	v_pk_fma_f32 v[66:67], v[158:159], v[42:43], v[66:67] op_sel_hi:[1,0,1]
	v_pk_fma_f32 v[68:69], v[160:161], v[42:43], v[68:69] op_sel_hi:[1,0,1]
	v_pk_fma_f32 v[70:71], v[162:163], v[42:43], v[70:71] op_sel_hi:[1,0,1]
	v_pk_fma_f32 v[32:33], v[164:165], v[42:43], v[32:33] op_sel_hi:[1,0,1]
	s_waitcnt lgkmcnt(4)
	v_cvt_pk_f32_fp8_e32 v[198:199], v138
	v_cvt_pk_f32_fp8_sdwa v[200:201], v138 src0_sel:WORD_1
	v_cvt_pk_f32_fp8_e32 v[202:203], v139
	v_cvt_pk_f32_fp8_sdwa v[138:139], v139 src0_sel:WORD_1
	v_pk_fma_f32 v[66:67], v[166:167], v[44:45], v[66:67] op_sel_hi:[1,0,1]
	v_pk_fma_f32 v[68:69], v[168:169], v[44:45], v[68:69] op_sel_hi:[1,0,1]
	v_pk_fma_f32 v[70:71], v[170:171], v[44:45], v[70:71] op_sel_hi:[1,0,1]
	v_pk_fma_f32 v[32:33], v[172:173], v[44:45], v[32:33] op_sel_hi:[1,0,1]
	v_pk_fma_f32 v[66:67], v[180:181], v[46:47], v[66:67] op_sel_hi:[1,0,1]
	v_pk_fma_f32 v[68:69], v[182:183], v[46:47], v[68:69] op_sel_hi:[1,0,1]
	v_pk_fma_f32 v[70:71], v[184:185], v[46:47], v[70:71] op_sel_hi:[1,0,1]
	v_pk_fma_f32 v[32:33], v[50:51], v[46:47], v[32:33] op_sel_hi:[1,0,1]
	s_waitcnt lgkmcnt(3)
	v_cvt_pk_f32_fp8_e32 v[34:35], v140
	v_cvt_pk_f32_fp8_sdwa v[36:37], v140 src0_sel:WORD_1
	v_cvt_pk_f32_fp8_e32 v[38:39], v141
	v_cvt_pk_f32_fp8_sdwa v[40:41], v141 src0_sel:WORD_1
	s_waitcnt lgkmcnt(2)
	v_cvt_pk_f32_fp8_e32 v[42:43], v174
	v_cvt_pk_f32_fp8_sdwa v[44:45], v174 src0_sel:WORD_1
	v_cvt_pk_f32_fp8_e32 v[46:47], v175
	v_cvt_pk_f32_fp8_sdwa v[48:49], v175 src0_sel:WORD_1
	s_waitcnt lgkmcnt(1)
	v_cvt_pk_f32_fp8_e32 v[50:51], v176
	v_cvt_pk_f32_fp8_sdwa v[72:73], v176 src0_sel:WORD_1
	v_cvt_pk_f32_fp8_e32 v[74:75], v177
	v_cvt_pk_f32_fp8_sdwa v[118:119], v177 src0_sel:WORD_1
	s_waitcnt lgkmcnt(0)
	v_cvt_pk_f32_fp8_e32 v[120:121], v178
	v_cvt_pk_f32_fp8_sdwa v[122:123], v178 src0_sel:WORD_1
	v_cvt_pk_f32_fp8_e32 v[124:125], v179
	v_pk_fma_f32 v[66:67], v[186:187], v[26:27], v[66:67] op_sel_hi:[1,0,1]
	v_pk_fma_f32 v[68:69], v[188:189], v[26:27], v[68:69] op_sel_hi:[1,0,1]
	v_pk_fma_f32 v[70:71], v[190:191], v[26:27], v[70:71] op_sel_hi:[1,0,1]
	v_pk_fma_f32 v[26:27], v[52:53], v[26:27], v[32:33] op_sel_hi:[1,0,1]
	v_pk_fma_f32 v[66:67], v[192:193], v[28:29], v[66:67] op_sel_hi:[1,0,1]
	v_pk_fma_f32 v[68:69], v[194:195], v[28:29], v[68:69] op_sel_hi:[1,0,1]
	v_pk_fma_f32 v[70:71], v[196:197], v[28:29], v[70:71] op_sel_hi:[1,0,1]
	v_pk_fma_f32 v[26:27], v[64:65], v[28:29], v[26:27] op_sel_hi:[1,0,1]
	v_pk_fma_f32 v[66:67], v[198:199], v[30:31], v[66:67] op_sel_hi:[1,0,1]
	v_pk_fma_f32 v[68:69], v[200:201], v[30:31], v[68:69] op_sel_hi:[1,0,1]
	v_pk_fma_f32 v[70:71], v[202:203], v[30:31], v[70:71] op_sel_hi:[1,0,1]
	v_pk_fma_f32 v[26:27], v[138:139], v[30:31], v[26:27] op_sel_hi:[1,0,1]
	v_cvt_pk_f32_fp8_sdwa v[126:127], v179 src0_sel:WORD_1
	s_setprio 0
	s_waitcnt vmcnt(32)
	v_and_b32_e32 v9, 0x1fff8, v14
	v_and_b32_e32 v11, 0x1fff8, v18
	v_and_b32_e32 v13, 0x1fff8, v20
	v_and_b32_e32 v15, 0x1fff8, v22
	ds_read_b64 v[28:29], v9
	ds_read_b64 v[30:31], v11
	ds_read_b64 v[32:33], v13
	ds_read_b64 v[52:53], v15
	v_and_b32_e32 v9, 0x1fff8, v24
	v_and_b32_e32 v11, 0x1fff8, v12
	v_and_b32_e32 v13, 0x1fff8, v16
	v_and_b32_e32 v15, 0x1fff8, v7
	ds_read_b64 v[64:65], v9
	ds_read_b64 v[128:129], v11
	ds_read_b64 v[130:131], v13
	ds_read_b64 v[132:133], v15
	s_setprio 1
	s_waitcnt lgkmcnt(7)
	v_cvt_pk_f32_fp8_e32 v[134:135], v28
	v_pk_fma_f32 v[34:35], v[34:35], v[4:5], v[66:67] op_sel_hi:[1,0,1]
	s_waitcnt lgkmcnt(6)
	v_cvt_pk_f32_fp8_e32 v[140:141], v30
	v_pk_fma_f32 v[34:35], v[42:43], v[6:7], v[34:35] op_sel_hi:[1,0,1]
	s_waitcnt lgkmcnt(5)
	v_cvt_pk_f32_fp8_e32 v[146:147], v32
	v_pk_fma_f32 v[34:35], v[50:51], v[8:9], v[34:35] op_sel_hi:[1,0,1]
	s_waitcnt lgkmcnt(4)
	v_cvt_pk_f32_fp8_e32 v[152:153], v52
	v_pk_fma_f32 v[34:35], v[120:121], v[10:11], v[34:35] op_sel_hi:[1,0,1]
	s_waitcnt lgkmcnt(3)
	v_cvt_pk_f32_fp8_e32 v[158:159], v64
	v_pk_fma_f32 v[34:35], v[134:135], v[14:15], v[34:35] op_sel_hi:[1,0,1]
	s_waitcnt lgkmcnt(2)
	v_cvt_pk_f32_fp8_e32 v[164:165], v128
	v_pk_fma_f32 v[34:35], v[140:141], v[18:19], v[34:35] op_sel_hi:[1,0,1]
	s_waitcnt lgkmcnt(1)
	v_cvt_pk_f32_fp8_e32 v[170:171], v130
	v_pk_fma_f32 v[34:35], v[146:147], v[20:21], v[34:35] op_sel_hi:[1,0,1]
	v_cvt_pk_f32_fp8_sdwa v[136:137], v28 src0_sel:WORD_1
	v_pk_fma_f32 v[34:35], v[152:153], v[22:23], v[34:35] op_sel_hi:[1,0,1]
	v_cvt_pk_f32_fp8_sdwa v[142:143], v30 src0_sel:WORD_1
	v_pk_fma_f32 v[34:35], v[158:159], v[24:25], v[34:35] op_sel_hi:[1,0,1]
	v_cvt_pk_f32_fp8_sdwa v[148:149], v32 src0_sel:WORD_1
	v_pk_fma_f32 v[34:35], v[164:165], v[12:13], v[34:35] op_sel_hi:[1,0,1]
	v_cvt_pk_f32_fp8_sdwa v[154:155], v52 src0_sel:WORD_1
	v_pk_fma_f32 v[120:121], v[170:171], v[16:17], v[34:35] op_sel_hi:[1,0,1]
	v_pk_fma_f32 v[34:35], v[36:37], v[4:5], v[68:69] op_sel_hi:[1,0,1]
	v_cvt_pk_f32_fp8_sdwa v[160:161], v64 src0_sel:WORD_1
	v_pk_fma_f32 v[34:35], v[44:45], v[6:7], v[34:35] op_sel_hi:[1,0,1]
	v_cvt_pk_f32_fp8_sdwa v[166:167], v128 src0_sel:WORD_1
	v_pk_fma_f32 v[34:35], v[72:73], v[8:9], v[34:35] op_sel_hi:[1,0,1]
	v_cvt_pk_f32_fp8_sdwa v[172:173], v130 src0_sel:WORD_1
	v_pk_fma_f32 v[34:35], v[122:123], v[10:11], v[34:35] op_sel_hi:[1,0,1]
	v_cvt_pk_f32_fp8_e32 v[138:139], v29
	v_pk_fma_f32 v[34:35], v[136:137], v[14:15], v[34:35] op_sel_hi:[1,0,1]
	v_cvt_pk_f32_fp8_sdwa v[28:29], v29 src0_sel:WORD_1
	v_pk_fma_f32 v[34:35], v[142:143], v[18:19], v[34:35] op_sel_hi:[1,0,1]
	v_cvt_pk_f32_fp8_e32 v[144:145], v31
	v_pk_fma_f32 v[34:35], v[148:149], v[20:21], v[34:35] op_sel_hi:[1,0,1]
	v_pk_fma_f32 v[26:27], v[40:41], v[4:5], v[26:27] op_sel_hi:[1,0,1]
	v_pk_fma_f32 v[34:35], v[154:155], v[22:23], v[34:35] op_sel_hi:[1,0,1]
	v_cvt_pk_f32_fp8_sdwa v[30:31], v31 src0_sel:WORD_1
	v_pk_fma_f32 v[34:35], v[160:161], v[24:25], v[34:35] op_sel_hi:[1,0,1]
	v_cvt_pk_f32_fp8_e32 v[150:151], v33
	v_pk_fma_f32 v[34:35], v[166:167], v[12:13], v[34:35] op_sel_hi:[1,0,1]
	v_pk_fma_f32 v[26:27], v[48:49], v[6:7], v[26:27] op_sel_hi:[1,0,1]
	v_pk_fma_f32 v[122:123], v[172:173], v[16:17], v[34:35] op_sel_hi:[1,0,1]
	v_pk_fma_f32 v[34:35], v[38:39], v[4:5], v[70:71] op_sel_hi:[1,0,1]
	v_cvt_pk_f32_fp8_sdwa v[32:33], v33 src0_sel:WORD_1
	v_pk_fma_f32 v[34:35], v[46:47], v[6:7], v[34:35] op_sel_hi:[1,0,1]
	v_cvt_pk_f32_fp8_e32 v[156:157], v53
	v_pk_fma_f32 v[34:35], v[74:75], v[8:9], v[34:35] op_sel_hi:[1,0,1]
	v_pk_fma_f32 v[8:9], v[118:119], v[8:9], v[26:27] op_sel_hi:[1,0,1]
	v_pk_fma_f32 v[34:35], v[124:125], v[10:11], v[34:35] op_sel_hi:[1,0,1]
	v_cvt_pk_f32_fp8_sdwa v[52:53], v53 src0_sel:WORD_1
	v_cvt_pk_f32_fp8_e32 v[162:163], v65
	v_pk_fma_f32 v[34:35], v[138:139], v[14:15], v[34:35] op_sel_hi:[1,0,1]
	v_pk_fma_f32 v[8:9], v[126:127], v[10:11], v[8:9] op_sel_hi:[1,0,1]
	v_cvt_pk_f32_fp8_sdwa v[64:65], v65 src0_sel:WORD_1
	v_cvt_pk_f32_fp8_e32 v[168:169], v129
	v_pk_fma_f32 v[34:35], v[144:145], v[18:19], v[34:35] op_sel_hi:[1,0,1]
	v_pk_fma_f32 v[8:9], v[28:29], v[14:15], v[8:9] op_sel_hi:[1,0,1]
	v_cvt_pk_f32_fp8_sdwa v[128:129], v129 src0_sel:WORD_1
	v_cvt_pk_f32_fp8_e32 v[174:175], v131
	v_pk_fma_f32 v[34:35], v[150:151], v[20:21], v[34:35] op_sel_hi:[1,0,1]
	v_pk_fma_f32 v[8:9], v[30:31], v[18:19], v[8:9] op_sel_hi:[1,0,1]
	v_cvt_pk_f32_fp8_sdwa v[130:131], v131 src0_sel:WORD_1
	v_pk_fma_f32 v[34:35], v[156:157], v[22:23], v[34:35] op_sel_hi:[1,0,1]
	v_pk_fma_f32 v[8:9], v[32:33], v[20:21], v[8:9] op_sel_hi:[1,0,1]
	s_waitcnt lgkmcnt(0)
	v_cvt_pk_f32_fp8_e32 v[118:119], v132
	v_pk_fma_f32 v[34:35], v[162:163], v[24:25], v[34:35] op_sel_hi:[1,0,1]
	v_pk_fma_f32 v[8:9], v[52:53], v[22:23], v[8:9] op_sel_hi:[1,0,1]
	v_pk_fma_f32 v[34:35], v[168:169], v[12:13], v[34:35] op_sel_hi:[1,0,1]
	v_pk_fma_f32 v[8:9], v[64:65], v[24:25], v[8:9] op_sel_hi:[1,0,1]
	v_pk_fma_f32 v[124:125], v[174:175], v[16:17], v[34:35] op_sel_hi:[1,0,1]
	v_pk_fma_f32 v[8:9], v[128:129], v[12:13], v[8:9] op_sel_hi:[1,0,1]
	v_cvt_pk_f32_fp8_sdwa v[126:127], v132 src0_sel:WORD_1
	v_cvt_pk_f32_fp8_e32 v[134:135], v133
	v_cvt_pk_f32_fp8_sdwa v[132:133], v133 src0_sel:WORD_1
	v_pk_fma_f32 v[128:129], v[130:131], v[16:17], v[8:9] op_sel_hi:[1,0,1]
	v_mov_b32_e32 v130, v7
	s_setprio 0
	s_add_i32 s18, s18, 2
	s_cmp_gt_u32 s17, 61
	s_cselect_b64 s[10:11], -1, 0
	s_cmp_lt_u32 s17, 62
	s_cselect_b32 s19, s18, 63
	s_lshl_b32 s20, s19, 1
	s_and_b32 s20, s20, 0xf8
	s_add_i32 s20, s20, s4
	s_ashr_i32 s21, s20, 31
	s_lshl_b64 s[20:21], s[20:21], 15
	s_add_u32 s20, s12, s20
	s_addc_u32 s21, s13, s21
	s_lshl_b32 s19, s19, 13
	s_and_b32 s19, s19, 0x6000
	s_add_u32 s20, s20, s19
	s_addc_u32 s21, s21, 0
	s_add_u32 s66, s20, s5
	s_addc_u32 s67, s21, 0
	global_load_dword v64, v2, s[20:21]
	global_load_dword v66, v2, s[20:21] offset:256
	global_load_dword v68, v2, s[20:21] offset:512
	global_load_dword v70, v2, s[20:21] offset:768
	global_load_dword v72, v2, s[20:21] offset:1024
	global_load_dword v74, v2, s[20:21] offset:1280
	global_load_dword v48, v2, s[20:21] offset:1536
	global_load_dword v50, v2, s[20:21] offset:1792
	global_load_dword v52, v2, s[20:21] offset:2048
	global_load_dword v32, v2, s[20:21] offset:2304
	global_load_dword v34, v2, s[20:21] offset:2560
	global_load_dword v36, v2, s[20:21] offset:2816
	global_load_dword v38, v2, s[20:21] offset:3072
	global_load_dword v40, v2, s[20:21] offset:3328
	global_load_dword v42, v2, s[20:21] offset:3584
	global_load_dword v44, v2, s[20:21] offset:3840
	global_load_dword v46, v2, s[66:67]
	global_load_dword v26, v2, s[66:67] offset:256
	global_load_dword v28, v2, s[66:67] offset:512
	global_load_dword v30, v2, s[66:67] offset:768
	global_load_dword v4, v2, s[66:67] offset:1024
	global_load_dword v6, v2, s[66:67] offset:1280
	global_load_dword v8, v2, s[66:67] offset:1536
	global_load_dword v10, v2, s[66:67] offset:1792
	global_load_dword v14, v2, s[66:67] offset:2048
	global_load_dword v18, v2, s[66:67] offset:2304
	global_load_dword v20, v2, s[66:67] offset:2560
	global_load_dword v22, v2, s[66:67] offset:2816
	global_load_dword v24, v2, s[66:67] offset:3072
	global_load_dword v12, v2, s[66:67] offset:3328
	global_load_dword v16, v2, s[66:67] offset:3584
	global_load_dword v7, v2, s[66:67] offset:3840
	s_waitcnt vmcnt(55)
	v_and_b32_e32 v9, 0x1fff8, v116
	v_and_b32_e32 v11, 0x1fff8, v104
	v_and_b32_e32 v13, 0x1fff8, v106
	v_and_b32_e32 v15, 0x1fff8, v108
	ds_read_b64 v[136:137], v9
	ds_read_b64 v[138:139], v11
	ds_read_b64 v[140:141], v13
	ds_read_b64 v[142:143], v15
	v_and_b32_e32 v9, 0x1fff8, v110
	v_and_b32_e32 v11, 0x1fff8, v112
	v_and_b32_e32 v13, 0x1fff8, v114
	v_and_b32_e32 v15, 0x1fff8, v98
	ds_read_b64 v[144:145], v9
	ds_read_b64 v[146:147], v11
	ds_read_b64 v[148:149], v13
	ds_read_b64 v[150:151], v15
	s_setprio 1
	s_waitcnt lgkmcnt(7)
	v_cvt_pk_f32_fp8_e32 v[152:153], v136
	v_cvt_pk_f32_fp8_sdwa v[154:155], v136 src0_sel:WORD_1
	v_cvt_pk_f32_fp8_e32 v[156:157], v137
	v_cvt_pk_f32_fp8_sdwa v[136:137], v137 src0_sel:WORD_1
	s_waitcnt lgkmcnt(6)
	v_cvt_pk_f32_fp8_e32 v[158:159], v138
	v_cvt_pk_f32_fp8_sdwa v[160:161], v138 src0_sel:WORD_1
	v_cvt_pk_f32_fp8_e32 v[162:163], v139
	v_cvt_pk_f32_fp8_sdwa v[138:139], v139 src0_sel:WORD_1
	s_waitcnt lgkmcnt(5)
	v_cvt_pk_f32_fp8_e32 v[164:165], v140
	v_cvt_pk_f32_fp8_sdwa v[166:167], v140 src0_sel:WORD_1
	v_cvt_pk_f32_fp8_e32 v[168:169], v141
	v_cvt_pk_f32_fp8_sdwa v[140:141], v141 src0_sel:WORD_1
	s_waitcnt lgkmcnt(4)
	v_cvt_pk_f32_fp8_e32 v[170:171], v142
	v_cvt_pk_f32_fp8_sdwa v[172:173], v142 src0_sel:WORD_1
	v_cvt_pk_f32_fp8_e32 v[174:175], v143
	v_cvt_pk_f32_fp8_sdwa v[142:143], v143 src0_sel:WORD_1
	s_waitcnt lgkmcnt(3)
	v_cvt_pk_f32_fp8_e32 v[176:177], v144
	v_cvt_pk_f32_fp8_sdwa v[178:179], v144 src0_sel:WORD_1
	v_cvt_pk_f32_fp8_e32 v[180:181], v145
	v_cvt_pk_f32_fp8_sdwa v[144:145], v145 src0_sel:WORD_1
	s_waitcnt lgkmcnt(2)
	v_cvt_pk_f32_fp8_e32 v[182:183], v146
	v_cvt_pk_f32_fp8_sdwa v[184:185], v146 src0_sel:WORD_1
	v_cvt_pk_f32_fp8_e32 v[186:187], v147
	v_cvt_pk_f32_fp8_sdwa v[146:147], v147 src0_sel:WORD_1
	s_waitcnt lgkmcnt(1)
	v_cvt_pk_f32_fp8_e32 v[188:189], v148
	v_cvt_pk_f32_fp8_sdwa v[190:191], v148 src0_sel:WORD_1
	v_cvt_pk_f32_fp8_e32 v[192:193], v149
	v_cvt_pk_f32_fp8_sdwa v[148:149], v149 src0_sel:WORD_1
	s_waitcnt lgkmcnt(0)
	v_cvt_pk_f32_fp8_e32 v[194:195], v150
	v_cvt_pk_f32_fp8_sdwa v[196:197], v150 src0_sel:WORD_1
	v_cvt_pk_f32_fp8_e32 v[198:199], v151
	v_cvt_pk_f32_fp8_sdwa v[150:151], v151 src0_sel:WORD_1
	s_setprio 0
	v_and_b32_e32 v9, 0x1fff8, v100
	s_waitcnt vmcnt(48)
	v_and_b32_e32 v11, 0x1fff8, v102
	v_and_b32_e32 v13, 0x1fff8, v78
	v_and_b32_e32 v15, 0x1fff8, v80
	ds_read_b64 v[200:201], v9
	ds_read_b64 v[202:203], v11
	ds_read_b64 v[204:205], v13
	ds_read_b64 v[206:207], v15
	v_and_b32_e32 v9, 0x1fff8, v82
	v_and_b32_e32 v11, 0x1fff8, v84
	v_and_b32_e32 v13, 0x1fff8, v86
	v_and_b32_e32 v15, 0x1fff8, v88
	ds_read_b64 v[208:209], v9
	ds_read_b64 v[210:211], v11
	ds_read_b64 v[212:213], v13
	ds_read_b64 v[214:215], v15
	s_setprio 1
	v_pk_fma_f32 v[118:119], v[118:119], v[130:131], v[120:121] op_sel_hi:[1,0,1]
	v_pk_fma_f32 v[120:121], v[126:127], v[130:131], v[122:123] op_sel_hi:[1,0,1]
	v_pk_fma_f32 v[122:123], v[134:135], v[130:131], v[124:125] op_sel_hi:[1,0,1]
	v_pk_fma_f32 v[118:119], v[152:153], v[116:117], v[118:119] op_sel_hi:[1,0,1]
	v_pk_fma_f32 v[120:121], v[154:155], v[116:117], v[120:121] op_sel_hi:[1,0,1]
	v_pk_fma_f32 v[122:123], v[156:157], v[116:117], v[122:123] op_sel_hi:[1,0,1]
	v_pk_fma_f32 v[124:125], v[132:133], v[130:131], v[128:129] op_sel_hi:[1,0,1]
	v_pk_fma_f32 v[118:119], v[158:159], v[104:105], v[118:119] op_sel_hi:[1,0,1]
	v_pk_fma_f32 v[120:121], v[160:161], v[104:105], v[120:121] op_sel_hi:[1,0,1]
	v_pk_fma_f32 v[122:123], v[162:163], v[104:105], v[122:123] op_sel_hi:[1,0,1]
	v_pk_fma_f32 v[116:117], v[136:137], v[116:117], v[124:125] op_sel_hi:[1,0,1]
	v_pk_fma_f32 v[118:119], v[164:165], v[106:107], v[118:119] op_sel_hi:[1,0,1]
	v_pk_fma_f32 v[120:121], v[166:167], v[106:107], v[120:121] op_sel_hi:[1,0,1]
	v_pk_fma_f32 v[122:123], v[168:169], v[106:107], v[122:123] op_sel_hi:[1,0,1]
	v_pk_fma_f32 v[104:105], v[138:139], v[104:105], v[116:117] op_sel_hi:[1,0,1]
	v_pk_fma_f32 v[118:119], v[170:171], v[108:109], v[118:119] op_sel_hi:[1,0,1]
	v_pk_fma_f32 v[120:121], v[172:173], v[108:109], v[120:121] op_sel_hi:[1,0,1]
	v_pk_fma_f32 v[122:123], v[174:175], v[108:109], v[122:123] op_sel_hi:[1,0,1]
	v_pk_fma_f32 v[104:105], v[140:141], v[106:107], v[104:105] op_sel_hi:[1,0,1]
	s_waitcnt lgkmcnt(7)
	v_cvt_pk_f32_fp8_e32 v[216:217], v200
	v_cvt_pk_f32_fp8_sdwa v[218:219], v200 src0_sel:WORD_1
	v_cvt_pk_f32_fp8_e32 v[220:221], v201
	v_pk_fma_f32 v[118:119], v[176:177], v[110:111], v[118:119] op_sel_hi:[1,0,1]
	v_pk_fma_f32 v[120:121], v[178:179], v[110:111], v[120:121] op_sel_hi:[1,0,1]
	v_pk_fma_f32 v[122:123], v[180:181], v[110:111], v[122:123] op_sel_hi:[1,0,1]
	v_pk_fma_f32 v[104:105], v[142:143], v[108:109], v[104:105] op_sel_hi:[1,0,1]
	v_cvt_pk_f32_fp8_sdwa v[200:201], v201 src0_sel:WORD_1
	s_waitcnt lgkmcnt(6)
	v_cvt_pk_f32_fp8_e32 v[222:223], v202
	v_cvt_pk_f32_fp8_sdwa v[224:225], v202 src0_sel:WORD_1
	v_cvt_pk_f32_fp8_e32 v[226:227], v203
	v_pk_fma_f32 v[118:119], v[182:183], v[112:113], v[118:119] op_sel_hi:[1,0,1]
	v_pk_fma_f32 v[120:121], v[184:185], v[112:113], v[120:121] op_sel_hi:[1,0,1]
	v_pk_fma_f32 v[122:123], v[186:187], v[112:113], v[122:123] op_sel_hi:[1,0,1]
	v_pk_fma_f32 v[104:105], v[144:145], v[110:111], v[104:105] op_sel_hi:[1,0,1]
	v_cvt_pk_f32_fp8_sdwa v[202:203], v203 src0_sel:WORD_1
	v_pk_fma_f32 v[118:119], v[188:189], v[114:115], v[118:119] op_sel_hi:[1,0,1]
	v_pk_fma_f32 v[120:121], v[190:191], v[114:115], v[120:121] op_sel_hi:[1,0,1]
	v_pk_fma_f32 v[122:123], v[192:193], v[114:115], v[122:123] op_sel_hi:[1,0,1]
	v_pk_fma_f32 v[104:105], v[146:147], v[112:113], v[104:105] op_sel_hi:[1,0,1]
	s_waitcnt lgkmcnt(4)
	v_cvt_pk_f32_fp8_e32 v[124:125], v207
	v_pk_fma_f32 v[118:119], v[194:195], v[98:99], v[118:119] op_sel_hi:[1,0,1]
	v_pk_fma_f32 v[120:121], v[196:197], v[98:99], v[120:121] op_sel_hi:[1,0,1]
	v_pk_fma_f32 v[122:123], v[198:199], v[98:99], v[122:123] op_sel_hi:[1,0,1]
	v_pk_fma_f32 v[104:105], v[148:149], v[114:115], v[104:105] op_sel_hi:[1,0,1]
	v_pk_fma_f32 v[118:119], v[216:217], v[100:101], v[118:119] op_sel_hi:[1,0,1]
	v_pk_fma_f32 v[120:121], v[218:219], v[100:101], v[120:121] op_sel_hi:[1,0,1]
	v_pk_fma_f32 v[122:123], v[220:221], v[100:101], v[122:123] op_sel_hi:[1,0,1]
	v_pk_fma_f32 v[98:99], v[150:151], v[98:99], v[104:105] op_sel_hi:[1,0,1]
	v_pk_fma_f32 v[118:119], v[222:223], v[102:103], v[118:119] op_sel_hi:[1,0,1]
	v_pk_fma_f32 v[120:121], v[224:225], v[102:103], v[120:121] op_sel_hi:[1,0,1]
	v_pk_fma_f32 v[122:123], v[226:227], v[102:103], v[122:123] op_sel_hi:[1,0,1]
	v_pk_fma_f32 v[98:99], v[200:201], v[100:101], v[98:99] op_sel_hi:[1,0,1]
	v_cvt_pk_f32_fp8_e32 v[106:107], v204
	v_cvt_pk_f32_fp8_sdwa v[108:109], v204 src0_sel:WORD_1
	v_cvt_pk_f32_fp8_e32 v[110:111], v205
	v_cvt_pk_f32_fp8_sdwa v[112:113], v205 src0_sel:WORD_1
	v_cvt_pk_f32_fp8_e32 v[114:115], v206
	v_cvt_pk_f32_fp8_sdwa v[116:117], v206 src0_sel:WORD_1
	v_cvt_pk_f32_fp8_sdwa v[126:127], v207 src0_sel:WORD_1
	s_waitcnt lgkmcnt(3)
	v_cvt_pk_f32_fp8_e32 v[128:129], v208
	v_cvt_pk_f32_fp8_sdwa v[130:131], v208 src0_sel:WORD_1
	v_cvt_pk_f32_fp8_e32 v[132:133], v209
	v_cvt_pk_f32_fp8_sdwa v[134:135], v209 src0_sel:WORD_1
	s_waitcnt lgkmcnt(2)
	v_cvt_pk_f32_fp8_e32 v[136:137], v210
	v_cvt_pk_f32_fp8_sdwa v[138:139], v210 src0_sel:WORD_1
	v_cvt_pk_f32_fp8_e32 v[140:141], v211
	v_cvt_pk_f32_fp8_sdwa v[142:143], v211 src0_sel:WORD_1
	s_waitcnt lgkmcnt(1)
	v_cvt_pk_f32_fp8_e32 v[144:145], v212
	v_cvt_pk_f32_fp8_sdwa v[146:147], v212 src0_sel:WORD_1
	v_cvt_pk_f32_fp8_e32 v[148:149], v213
	v_cvt_pk_f32_fp8_sdwa v[152:153], v213 src0_sel:WORD_1
	s_waitcnt lgkmcnt(0)
	v_cvt_pk_f32_fp8_e32 v[154:155], v214
	v_cvt_pk_f32_fp8_sdwa v[156:157], v214 src0_sel:WORD_1
	v_cvt_pk_f32_fp8_e32 v[158:159], v215
	v_cvt_pk_f32_fp8_sdwa v[160:161], v215 src0_sel:WORD_1
	v_pk_fma_f32 v[98:99], v[202:203], v[102:103], v[98:99] op_sel_hi:[1,0,1]
	s_setprio 0
	s_waitcnt vmcnt(40)
	v_and_b32_e32 v9, 0x1fff8, v90
	v_and_b32_e32 v11, 0x1fff8, v92
	v_and_b32_e32 v13, 0x1fff8, v94
	v_and_b32_e32 v15, 0x1fff8, v96
	ds_read_b64 v[100:101], v9
	ds_read_b64 v[102:103], v11
	ds_read_b64 v[104:105], v13
	ds_read_b64 v[150:151], v15
	v_and_b32_e32 v9, 0x1fff8, v76
	v_and_b32_e32 v11, 0x1fff8, v77
	v_and_b32_e32 v13, 0x1fff8, v56
	v_and_b32_e32 v15, 0x1fff8, v57
	ds_read_b64 v[162:163], v9
	ds_read_b64 v[164:165], v11
	ds_read_b64 v[166:167], v13
	ds_read_b64 v[168:169], v15
	s_setprio 1
	v_pk_fma_f32 v[106:107], v[106:107], v[78:79], v[118:119] op_sel_hi:[1,0,1]
	v_pk_fma_f32 v[108:109], v[108:109], v[78:79], v[120:121] op_sel_hi:[1,0,1]
	v_pk_fma_f32 v[110:111], v[110:111], v[78:79], v[122:123] op_sel_hi:[1,0,1]
	v_pk_fma_f32 v[78:79], v[112:113], v[78:79], v[98:99] op_sel_hi:[1,0,1]
	v_pk_fma_f32 v[106:107], v[114:115], v[80:81], v[106:107] op_sel_hi:[1,0,1]
	v_pk_fma_f32 v[108:109], v[116:117], v[80:81], v[108:109] op_sel_hi:[1,0,1]
	v_pk_fma_f32 v[110:111], v[124:125], v[80:81], v[110:111] op_sel_hi:[1,0,1]
	v_pk_fma_f32 v[78:79], v[126:127], v[80:81], v[78:79] op_sel_hi:[1,0,1]
	s_waitcnt lgkmcnt(7)
	v_cvt_pk_f32_fp8_e32 v[170:171], v100
	v_cvt_pk_f32_fp8_sdwa v[172:173], v100 src0_sel:WORD_1
	v_cvt_pk_f32_fp8_e32 v[174:175], v101
	v_cvt_pk_f32_fp8_sdwa v[100:101], v101 src0_sel:WORD_1
	v_pk_fma_f32 v[106:107], v[128:129], v[82:83], v[106:107] op_sel_hi:[1,0,1]
	v_pk_fma_f32 v[108:109], v[130:131], v[82:83], v[108:109] op_sel_hi:[1,0,1]
	v_pk_fma_f32 v[110:111], v[132:133], v[82:83], v[110:111] op_sel_hi:[1,0,1]
	v_pk_fma_f32 v[78:79], v[134:135], v[82:83], v[78:79] op_sel_hi:[1,0,1]
	s_waitcnt lgkmcnt(6)
	v_cvt_pk_f32_fp8_e32 v[176:177], v102
	v_cvt_pk_f32_fp8_sdwa v[178:179], v102 src0_sel:WORD_1
	v_cvt_pk_f32_fp8_e32 v[180:181], v103
	v_cvt_pk_f32_fp8_sdwa v[102:103], v103 src0_sel:WORD_1
	v_pk_fma_f32 v[106:107], v[136:137], v[84:85], v[106:107] op_sel_hi:[1,0,1]
	v_pk_fma_f32 v[108:109], v[138:139], v[84:85], v[108:109] op_sel_hi:[1,0,1]
	v_pk_fma_f32 v[110:111], v[140:141], v[84:85], v[110:111] op_sel_hi:[1,0,1]
	v_pk_fma_f32 v[78:79], v[142:143], v[84:85], v[78:79] op_sel_hi:[1,0,1]
	s_waitcnt lgkmcnt(5)
	v_cvt_pk_f32_fp8_e32 v[182:183], v104
	v_cvt_pk_f32_fp8_sdwa v[184:185], v104 src0_sel:WORD_1
	v_cvt_pk_f32_fp8_e32 v[186:187], v105
	v_cvt_pk_f32_fp8_sdwa v[104:105], v105 src0_sel:WORD_1
	v_pk_fma_f32 v[106:107], v[144:145], v[86:87], v[106:107] op_sel_hi:[1,0,1]
	v_pk_fma_f32 v[108:109], v[146:147], v[86:87], v[108:109] op_sel_hi:[1,0,1]
	v_pk_fma_f32 v[110:111], v[148:149], v[86:87], v[110:111] op_sel_hi:[1,0,1]
	v_pk_fma_f32 v[78:79], v[152:153], v[86:87], v[78:79] op_sel_hi:[1,0,1]
	v_pk_fma_f32 v[106:107], v[154:155], v[88:89], v[106:107] op_sel_hi:[1,0,1]
	v_pk_fma_f32 v[108:109], v[156:157], v[88:89], v[108:109] op_sel_hi:[1,0,1]
	v_pk_fma_f32 v[110:111], v[158:159], v[88:89], v[110:111] op_sel_hi:[1,0,1]
	v_pk_fma_f32 v[78:79], v[160:161], v[88:89], v[78:79] op_sel_hi:[1,0,1]
	s_waitcnt lgkmcnt(3)
	v_cvt_pk_f32_fp8_e32 v[194:195], v162
	v_cvt_pk_f32_fp8_sdwa v[196:197], v162 src0_sel:WORD_1
	v_cvt_pk_f32_fp8_e32 v[198:199], v163
	v_cvt_pk_f32_fp8_sdwa v[162:163], v163 src0_sel:WORD_1
	s_waitcnt lgkmcnt(2)
	v_cvt_pk_f32_fp8_e32 v[200:201], v164
	v_cvt_pk_f32_fp8_sdwa v[202:203], v164 src0_sel:WORD_1
	v_cvt_pk_f32_fp8_e32 v[204:205], v165
	v_cvt_pk_f32_fp8_sdwa v[164:165], v165 src0_sel:WORD_1
	v_pk_fma_f32 v[106:107], v[170:171], v[90:91], v[106:107] op_sel_hi:[1,0,1]
	v_pk_fma_f32 v[108:109], v[172:173], v[90:91], v[108:109] op_sel_hi:[1,0,1]
	v_pk_fma_f32 v[110:111], v[174:175], v[90:91], v[110:111] op_sel_hi:[1,0,1]
	v_pk_fma_f32 v[78:79], v[100:101], v[90:91], v[78:79] op_sel_hi:[1,0,1]
	v_pk_fma_f32 v[106:107], v[176:177], v[92:93], v[106:107] op_sel_hi:[1,0,1]
	v_pk_fma_f32 v[108:109], v[178:179], v[92:93], v[108:109] op_sel_hi:[1,0,1]
	v_pk_fma_f32 v[110:111], v[180:181], v[92:93], v[110:111] op_sel_hi:[1,0,1]
	v_pk_fma_f32 v[78:79], v[102:103], v[92:93], v[78:79] op_sel_hi:[1,0,1]
	v_cvt_pk_f32_fp8_e32 v[188:189], v150
	v_cvt_pk_f32_fp8_sdwa v[190:191], v150 src0_sel:WORD_1
	v_cvt_pk_f32_fp8_e32 v[192:193], v151
	v_cvt_pk_f32_fp8_sdwa v[150:151], v151 src0_sel:WORD_1
	v_pk_fma_f32 v[106:107], v[182:183], v[94:95], v[106:107] op_sel_hi:[1,0,1]
	v_pk_fma_f32 v[108:109], v[184:185], v[94:95], v[108:109] op_sel_hi:[1,0,1]
	v_pk_fma_f32 v[110:111], v[186:187], v[94:95], v[110:111] op_sel_hi:[1,0,1]
	v_pk_fma_f32 v[78:79], v[104:105], v[94:95], v[78:79] op_sel_hi:[1,0,1]
	s_waitcnt lgkmcnt(1)
	v_cvt_pk_f32_fp8_sdwa v[88:89], v167 src0_sel:WORD_1
	s_waitcnt lgkmcnt(0)
	v_cvt_pk_f32_fp8_sdwa v[94:95], v169 src0_sel:WORD_1
	v_pk_fma_f32 v[78:79], v[162:163], v[76:77], v[78:79] op_sel_hi:[1,0,1]
	v_pk_fma_f32 v[106:107], v[188:189], v[96:97], v[106:107] op_sel_hi:[1,0,1]
	v_pk_fma_f32 v[108:109], v[190:191], v[96:97], v[108:109] op_sel_hi:[1,0,1]
	v_pk_fma_f32 v[110:111], v[192:193], v[96:97], v[110:111] op_sel_hi:[1,0,1]
	v_pk_fma_f32 v[78:79], v[150:151], v[96:97], v[78:79] op_sel_hi:[1,0,1]
	v_pk_fma_f32 v[78:79], v[88:89], v[56:57], v[78:79] op_sel_hi:[1,0,1]
	v_pk_fma_f32 v[106:107], v[194:195], v[76:77], v[106:107] op_sel_hi:[1,0,1]
	v_pk_fma_f32 v[108:109], v[196:197], v[76:77], v[108:109] op_sel_hi:[1,0,1]
	v_pk_fma_f32 v[110:111], v[198:199], v[76:77], v[110:111] op_sel_hi:[1,0,1]
	v_pk_fma_f32 v[78:79], v[164:165], v[76:77], v[78:79] op_sel:[0,1,0] op_sel_hi:[1,1,1]
	v_cvt_pk_f32_fp8_e32 v[82:83], v166
	v_cvt_pk_f32_fp8_sdwa v[84:85], v166 src0_sel:WORD_1
	v_cvt_pk_f32_fp8_e32 v[86:87], v167
	v_cvt_pk_f32_fp8_e32 v[90:91], v168
	v_cvt_pk_f32_fp8_sdwa v[92:93], v168 src0_sel:WORD_1
	v_cvt_pk_f32_fp8_e32 v[96:97], v169
	v_pk_fma_f32 v[78:79], v[94:95], v[56:57], v[78:79] op_sel:[0,1,0] op_sel_hi:[1,1,1]
	s_setprio 0
	s_waitcnt vmcnt(32)
	v_and_b32_e32 v9, 0x1fff8, v58
	v_and_b32_e32 v11, 0x1fff8, v59
	v_and_b32_e32 v13, 0x1fff8, v60
	v_and_b32_e32 v15, 0x1fff8, v61
	ds_read_b64 v[100:101], v9
	ds_read_b64 v[102:103], v11
	ds_read_b64 v[104:105], v13
	ds_read_b64 v[112:113], v15
	v_and_b32_e32 v9, 0x1fff8, v62
	v_and_b32_e32 v11, 0x1fff8, v63
	v_and_b32_e32 v13, 0x1fff8, v54
	v_and_b32_e32 v15, 0x1fff8, v55
	ds_read_b64 v[114:115], v9
	ds_read_b64 v[118:119], v11
	ds_read_b64 v[120:121], v13
	ds_read_b64 v[122:123], v15
	s_setprio 1
	s_waitcnt lgkmcnt(7)
	v_cvt_pk_f32_fp8_e32 v[124:125], v100
	v_cvt_pk_f32_fp8_sdwa v[126:127], v100 src0_sel:WORD_1
	v_cvt_pk_f32_fp8_e32 v[128:129], v101
	v_cvt_pk_f32_fp8_sdwa v[100:101], v101 src0_sel:WORD_1
	s_waitcnt lgkmcnt(6)
	v_cvt_pk_f32_fp8_sdwa v[134:135], v103 src0_sel:WORD_1
	v_cvt_pk_f32_fp8_e32 v[130:131], v102
	s_waitcnt lgkmcnt(5)
	v_cvt_pk_f32_fp8_e32 v[138:139], v104
	v_cvt_pk_f32_fp8_sdwa v[140:141], v104 src0_sel:WORD_1
	v_cvt_pk_f32_fp8_e32 v[142:143], v105
	v_cvt_pk_f32_fp8_sdwa v[104:105], v105 src0_sel:WORD_1
	s_waitcnt lgkmcnt(4)
	v_cvt_pk_f32_fp8_sdwa v[148:149], v113 src0_sel:WORD_1
	v_pk_fma_f32 v[106:107], v[200:201], v[76:77], v[106:107] op_sel:[0,1,0] op_sel_hi:[1,1,1]
	s_waitcnt lgkmcnt(3)
	v_cvt_pk_f32_fp8_e32 v[152:153], v114
	v_cvt_pk_f32_fp8_sdwa v[154:155], v114 src0_sel:WORD_1
	v_cvt_pk_f32_fp8_e32 v[156:157], v115
	v_cvt_pk_f32_fp8_sdwa v[114:115], v115 src0_sel:WORD_1
	s_waitcnt lgkmcnt(2)
	v_cvt_pk_f32_fp8_sdwa v[162:163], v119 src0_sel:WORD_1
	v_pk_fma_f32 v[82:83], v[82:83], v[56:57], v[106:107] op_sel_hi:[1,0,1]
	v_cvt_pk_f32_fp8_e32 v[144:145], v112
	v_cvt_pk_f32_fp8_e32 v[158:159], v118
	v_cvt_pk_f32_fp8_sdwa v[160:161], v118 src0_sel:WORD_1
	v_cvt_pk_f32_fp8_e32 v[164:165], v119
	s_waitcnt lgkmcnt(1)
	v_cvt_pk_f32_fp8_e32 v[118:119], v120
	v_cvt_pk_f32_fp8_sdwa v[168:169], v120 src0_sel:WORD_1
	v_cvt_pk_f32_fp8_e32 v[170:171], v121
	v_cvt_pk_f32_fp8_sdwa v[120:121], v121 src0_sel:WORD_1
	s_waitcnt lgkmcnt(0)
; #define GAS __attribute__((address_space(1)))
; __device__ __forceinline__ unsigned f2bf(float f) { unsigned u = __builtin_bit_cast(unsigned, f); return (u + 0x7fffu + ((u >> 16) & 1u)) >> 16; }
; template <int VVAR> __device__ __forceinline__ void peer_v_phase(LAS unsigned char* lds, int wave, int vcu, const unsigned char* __restrict__ VS_l, const unsigned* __restrict__ PW, bf16* __restrict__ Y) {
;     ...
; #pragma unroll 1
;     for (int it = 0; it < (VVAR == 5 ? 2 : 64); it += 2) {
;         V_HALF(pa, pb, it + 1);
;         V_HALF(pb, pa, it + 2);
;         if ((it & 3) == 2) {
;             const int blk = th * 128 + wave + 8 * (it >> 2);
;             bf16* yp = Y + ((size_t)blk * 1024 + cs * 8) * 64 + lane;
; #pragma unroll
;             for (int c = 0; c < 8; ++c) ((GAS unsigned short*)yp)[c * 64] = (unsigned short)f2bf(acc[c]);
; #pragma unroll
;             for (int c = 0; c < 8; ++c) acc[c] = 0.f;
	v_cvt_pk_f32_fp8_sdwa v[176:177], v123 src0_sel:WORD_1
	v_pk_fma_f32 v[82:83], v[90:91], v[56:57], v[82:83] op_sel:[0,1,0] op_sel_hi:[1,1,1]
	v_pk_fma_f32 v[78:79], v[100:101], v[58:59], v[78:79] op_sel_hi:[1,0,1]
	v_pk_fma_f32 v[78:79], v[134:135], v[58:59], v[78:79] op_sel:[0,1,0] op_sel_hi:[1,1,1]
	v_pk_fma_f32 v[82:83], v[124:125], v[58:59], v[82:83] op_sel_hi:[1,0,1]
	v_pk_fma_f32 v[78:79], v[104:105], v[60:61], v[78:79] op_sel_hi:[1,0,1]
	v_pk_fma_f32 v[78:79], v[148:149], v[60:61], v[78:79] op_sel:[0,1,0] op_sel_hi:[1,1,1]
	v_pk_fma_f32 v[82:83], v[130:131], v[58:59], v[82:83] op_sel:[0,1,0] op_sel_hi:[1,1,1]
	v_pk_fma_f32 v[78:79], v[114:115], v[62:63], v[78:79] op_sel_hi:[1,0,1]
	v_pk_fma_f32 v[78:79], v[162:163], v[62:63], v[78:79] op_sel:[0,1,0] op_sel_hi:[1,1,1]
	v_pk_fma_f32 v[82:83], v[138:139], v[60:61], v[82:83] op_sel_hi:[1,0,1]
	v_cvt_pk_f32_fp8_e32 v[172:173], v122
	v_pk_fma_f32 v[78:79], v[120:121], v[54:55], v[78:79] op_sel_hi:[1,0,1]
	v_pk_fma_f32 v[82:83], v[144:145], v[60:61], v[82:83] op_sel:[0,1,0] op_sel_hi:[1,1,1]
	v_pk_fma_f32 v[124:125], v[176:177], v[54:55], v[78:79] op_sel:[0,1,0] op_sel_hi:[1,1,1]
	v_pk_fma_f32 v[82:83], v[152:153], v[62:63], v[82:83] op_sel_hi:[1,0,1]
	v_pk_fma_f32 v[82:83], v[158:159], v[62:63], v[82:83] op_sel:[0,1,0] op_sel_hi:[1,1,1]
	v_pk_fma_f32 v[82:83], v[118:119], v[54:55], v[82:83] op_sel_hi:[1,0,1]
	v_cvt_pk_f32_fp8_sdwa v[132:133], v102 src0_sel:WORD_1
	v_cvt_pk_f32_fp8_e32 v[102:103], v103
	v_pk_fma_f32 v[118:119], v[172:173], v[54:55], v[82:83] op_sel:[0,1,0] op_sel_hi:[1,1,1]
	v_pk_fma_f32 v[82:83], v[202:203], v[76:77], v[108:109] op_sel:[0,1,0] op_sel_hi:[1,1,1]
	v_pk_fma_f32 v[76:77], v[204:205], v[76:77], v[110:111] op_sel:[0,1,0] op_sel_hi:[1,1,1]
	v_pk_fma_f32 v[82:83], v[84:85], v[56:57], v[82:83] op_sel_hi:[1,0,1]
	v_pk_fma_f32 v[228:229], v[86:87], v[56:57], v[76:77] op_sel_hi:[1,0,1]
	v_cvt_pk_f32_fp8_sdwa v[146:147], v112 src0_sel:WORD_1
	v_cvt_pk_f32_fp8_e32 v[112:113], v113
	v_pk_fma_f32 v[228:229], v[96:97], v[56:57], v[228:229] op_sel:[0,1,0] op_sel_hi:[1,1,1]
	v_pk_fma_f32 v[82:83], v[92:93], v[56:57], v[82:83] op_sel:[0,1,0] op_sel_hi:[1,1,1]
	v_pk_fma_f32 v[228:229], v[128:129], v[58:59], v[228:229] op_sel_hi:[1,0,1]
	v_pk_fma_f32 v[82:83], v[126:127], v[58:59], v[82:83] op_sel_hi:[1,0,1]
	v_pk_fma_f32 v[228:229], v[102:103], v[58:59], v[228:229] op_sel:[0,1,0] op_sel_hi:[1,1,1]
	v_cvt_pk_f32_fp8_e32 v[178:179], v123
	v_pk_fma_f32 v[228:229], v[142:143], v[60:61], v[228:229] op_sel_hi:[1,0,1]
	v_pk_fma_f32 v[82:83], v[132:133], v[58:59], v[82:83] op_sel:[0,1,0] op_sel_hi:[1,1,1]
	v_pk_fma_f32 v[228:229], v[112:113], v[60:61], v[228:229] op_sel:[0,1,0] op_sel_hi:[1,1,1]
	v_pk_fma_f32 v[82:83], v[140:141], v[60:61], v[82:83] op_sel_hi:[1,0,1]
	v_pk_fma_f32 v[228:229], v[156:157], v[62:63], v[228:229] op_sel_hi:[1,0,1]
	v_pk_fma_f32 v[82:83], v[146:147], v[60:61], v[82:83] op_sel:[0,1,0] op_sel_hi:[1,1,1]
	v_pk_fma_f32 v[228:229], v[164:165], v[62:63], v[228:229] op_sel:[0,1,0] op_sel_hi:[1,1,1]
	v_pk_fma_f32 v[82:83], v[154:155], v[62:63], v[82:83] op_sel_hi:[1,0,1]
	v_pk_fma_f32 v[228:229], v[170:171], v[54:55], v[228:229] op_sel_hi:[1,0,1]
	v_pk_fma_f32 v[82:83], v[160:161], v[62:63], v[82:83] op_sel:[0,1,0] op_sel_hi:[1,1,1]
	v_pk_fma_f32 v[120:121], v[178:179], v[54:55], v[228:229] op_sel:[0,1,0] op_sel_hi:[1,1,1]
	v_cvt_pk_f32_fp8_sdwa v[174:175], v122 src0_sel:WORD_1
	v_pk_fma_f32 v[82:83], v[168:169], v[54:55], v[82:83] op_sel_hi:[1,0,1]
	v_pk_fma_f32 v[122:123], v[174:175], v[54:55], v[82:83] op_sel:[0,1,0] op_sel_hi:[1,1,1]
	s_setprio 0
	s_bitcmp0_b32 s17, 1
	s_cbranch_scc1 .LBB0_955
	s_lshl_b64 s[8:9], s[8:9], 17
	v_lshl_add_u64 v[54:55], v[0:1], 0, s[8:9]
	v_cvt_pk_bf16_f32 v9, v118, v119
	v_cvt_pk_bf16_f32 v11, v122, v123
	v_cvt_pk_bf16_f32 v13, v120, v121
	v_cvt_pk_bf16_f32 v15, v124, v125
	global_store_short v[54:55], v9, off
	global_store_short_d16_hi v[54:55], v9, off offset:128
	global_store_short v[54:55], v11, off offset:256
	global_store_short_d16_hi v[54:55], v11, off offset:384
	global_store_short v[54:55], v13, off offset:512
	global_store_short_d16_hi v[54:55], v13, off offset:640
	global_store_short v[54:55], v15, off offset:768
	global_store_short_d16_hi v[54:55], v15, off offset:896
	v_mov_b64_e32 v[118:119], 0
	v_mov_b64_e32 v[122:123], 0
	v_mov_b64_e32 v[120:121], 0
	v_mov_b64_e32 v[124:125], 0
	s_branch .LBB0_955
